# v23 + one static s_setprio 1 for waves 4-7 during the attention phase (P3)
# speedup vs baseline: 1.0358x; 1.0358x over previous
; __device__ __forceinline__ void p3_attention(Frame& F) {
;     const int c = blockIdx.x; if (c >= 256) return;
;     const int xcd = c & 7, j = c >> 3, bh = xcd * 2 + (j >> 4), qb = j & 15, b = bh >> 3, h = bh & 7;
;     const bf16_t* KV = (const bf16_t*)(F.ws + WS_KV);
;     f32x16 o[4];
;     const int tid = F.tid, wid = tid >> 6, lane = tid & 63, r32 = lane & 31, hi = lane >> 5;
.LBB0_408:
	s_cmp_lt_i32 s34, 4
	s_cselect_b64 s[16:17], -1, 0
	s_cmpk_lt_i32 s2, 0x100
	s_cselect_b64 s[12:13], -1, 0
	s_and_b64 s[0:1], s[12:13], s[0:1]
	s_and_b64 s[0:1], s[16:17], s[0:1]
	s_andn2_b64 vcc, exec, s[0:1]
	s_cbranch_vccnz .LBB0_492
	v_readlane_b32 s99, v255, 8
	s_nop 3
	s_cmp_ge_u32 s99, 4
	s_cbranch_scc0 .Lp3_prio_done
	s_setprio 1
.Lp3_prio_done:
	v_mov_b32_e32 v1, 0
	s_mov_b64 s[0:1], 0
	v_mov_b32_e32 v194, 0
	v_mov_b32_e32 v195, v1

; __device__ __forceinline__ unsigned xb_ld(unsigned* p)              { return __hip_atomic_load(p, __ATOMIC_RELAXED, __HIP_MEMORY_SCOPE_AGENT); }
; __device__ __forceinline__ unsigned xb_add(unsigned* p, unsigned v) { return __hip_atomic_fetch_add(p, v, __ATOMIC_RELAXED, __HIP_MEMORY_SCOPE_AGENT); }
; __device__ __forceinline__ void xcd_barrier_complete(unsigned* bar, unsigned x, unsigned& nloc, unsigned& nx) {
;     const unsigned G = gridDim.x * gridDim.y * gridDim.z;
;     unsigned sum, cnt, mine, sp = 0u;
;     for (;;) {
;         sum = 0u; cnt = 0u; mine = 0u;
; #pragma unroll
;         for (unsigned j = 0; j < 16; ++j) { const unsigned c = xb_ld(&bar[XB_XCNT(j)]); sum += c; cnt += (c > 0u) ? 1u : 0u; mine = (j == x) ? c : mine; }
; __device__ __forceinline__ void xcd_barrier(const XcdBarrier& b) {
;     asm volatile("s_waitcnt vmcnt(0)" ::: "memory");
;     __syncthreads();
;     if (threadIdx.x == 0) {
;         unsigned* bar = b.bar;
;         __builtin_amdgcn_s_waitcnt(0);
;         unsigned nloc = b.st[0], nx = b.st[1];
;         if (nloc == 0u) { xcd_barrier_complete(bar, b.x, nloc, nx); b.st[0] = nloc; b.st[1] = nx; }
;         const unsigned old = xb_add(&bar[XB_XSUB(b.x)], 1u);
.LBB0_492:
	s_setprio 0
	s_cmp_gt_i32 s35, 4
	s_cselect_b64 s[0:1], -1, 0
	s_and_b64 s[4:5], s[16:17], s[0:1]
	s_andn2_b64 vcc, exec, s[4:5]
	v_readlane_b32 s56, v255, 7
	s_cbranch_vccnz .LBB0_542
	s_waitcnt vmcnt(0)
	v_cmp_eq_u32_e32 vcc, 0, v0
	s_waitcnt vmcnt(0)
	s_barrier
	s_and_saveexec_b64 s[4:5], vcc
	s_cbranch_execz .LBB0_541
	v_mov_b32_e32 v1, s56
	s_waitcnt vmcnt(0) expcnt(0) lgkmcnt(0)
	ds_read_b32 v3, v1
	ds_read_b32 v1, v1 offset:4
	s_waitcnt lgkmcnt(1)
	v_cmp_ne_u32_e32 vcc, 0, v3
	s_cbranch_vccnz .LBB0_509
	v_readlane_b32 s16, v255, 0
	v_readlane_b32 s17, v255, 1
	s_load_dwordx2 s[6:7], s[16:17], 0x4
	s_add_u32 s16, s82, 0x4200
	s_addc_u32 s17, s83, 0
	s_add_u32 s20, s82, 0x4400
	s_addc_u32 s21, s83, 0
	s_add_u32 s24, s82, 0x4500
	s_addc_u32 s25, s83, 0
	s_add_u32 s38, s82, 0x4600
	s_addc_u32 s39, s83, 0
	s_add_u32 s40, s82, 0x4700
	s_addc_u32 s41, s83, 0
	s_add_u32 s42, s82, 0x4800
	s_addc_u32 s43, s83, 0
	s_add_u32 s44, s82, 0x4900
	s_addc_u32 s45, s83, 0
	s_add_u32 s46, s82, 0x4a00
	s_addc_u32 s47, s83, 0
	s_add_u32 s48, s82, 0x4b00
	s_addc_u32 s49, s83, 0
	s_add_u32 s50, s82, 0x4c00
	s_addc_u32 s51, s83, 0
	s_add_u32 s52, s82, 0x4d00
	s_addc_u32 s53, s83, 0
	s_add_u32 s54, s82, 0x4e00
	s_addc_u32 s55, s83, 0
	s_add_u32 s56, s82, 0x4f00
	s_addc_u32 s57, s83, 0
	s_add_u32 s58, s82, 0x5000
	s_addc_u32 s59, s83, 0
	s_add_u32 s60, s82, 0x5100
	s_addc_u32 s61, s83, 0
	s_add_u32 s62, s82, 0x5200
	s_addc_u32 s63, s83, 0
	s_waitcnt lgkmcnt(0)
	s_mul_i32 s3, s6, s33
	s_add_u32 s64, s82, 0x5300
	s_mul_i32 s3, s3, s7
	s_addc_u32 s65, s83, 0
	s_mov_b32 s6, 1
	v_mov_b32_e32 v17, 0
	s_branch .LBB0_497
